# P11 X1 loads nt only
# baseline (speedup 1.0000x reference)
.LBB0_1286:
	s_add_u32 s0, s92, s8
	s_addc_u32 s1, s93, s9
	v_lshl_add_u64 v[24:25], s[92:93], 0, v[18:19]
	global_load_dwordx4 v[40:43], v36, s[0:1]
	v_add_co_u32_e32 v24, vcc, 0xe000000, v24
	v_mov_b32_e32 v27, v23
	s_nop 0
	v_addc_co_u32_e32 v25, vcc, 0, v25, vcc
	global_load_dwordx2 v[44:45], v[24:25], off offset:512 nt
	global_load_dwordx2 v[46:47], v[24:25], off offset:1024 nt
	global_load_dwordx2 v[48:49], v[24:25], off offset:1536 nt
	global_load_dwordx2 v[50:51], v[24:25], off nt
	v_mov_b32_e32 v29, v23
	s_add_i32 s2, s2, s4
	s_add_u32 s8, s8, s10
	s_addc_u32 s9, s9, s11
	v_lshl_add_u64 v[18:19], v[18:19], 0, s[6:7]
	s_cmp_lt_i32 s2, 0x8000
	s_waitcnt vmcnt(4)
	v_ashrrev_i32_e32 v25, 31, v40
	v_mov_b32_e32 v24, v40
	v_ashrrev_i32_e32 v53, 31, v41
	v_mov_b32_e32 v52, v41
	v_ashrrev_i32_e32 v41, 31, v42
	v_mov_b32_e32 v40, v42
	v_ashrrev_i32_e32 v55, 31, v43
	v_mov_b32_e32 v54, v43
	v_lshlrev_b64 v[24:25], 10, v[24:25]
	s_waitcnt vmcnt(1)
	v_lshlrev_b32_e32 v28, 16, v48
	v_and_b32_e32 v59, 0xffff0000, v48
	v_lshlrev_b32_e32 v43, 16, v49
	v_and_b32_e32 v57, 0xffff0000, v49
	v_lshlrev_b64 v[48:49], 10, v[52:53]
	v_lshlrev_b64 v[52:53], 10, v[54:55]
	v_lshlrev_b64 v[40:41], 10, v[40:41]
	v_lshl_add_u64 v[24:25], v[16:17], 0, v[24:25]
	v_lshl_add_u64 v[48:49], v[16:17], 0, v[48:49]
	v_lshl_add_u64 v[40:41], v[16:17], 0, v[40:41]
	v_lshl_add_u64 v[52:53], v[16:17], 0, v[52:53]
	global_load_dword v39, v[24:25], off
	global_load_dword v58, v[24:25], off offset:256
	global_load_dword v61, v[24:25], off offset:512
	global_load_dword v63, v[24:25], off offset:768
	global_load_dword v65, v[48:49], off
	global_load_dword v67, v[48:49], off offset:256
	global_load_dword v68, v[48:49], off offset:512
	global_load_dword v79, v[48:49], off offset:768
	global_load_dword v80, v[40:41], off
	global_load_dword v82, v[40:41], off offset:256
	global_load_dword v91, v[40:41], off offset:512
	global_load_dword v93, v[40:41], off offset:768
	global_load_dword v95, v[52:53], off
	global_load_dword v97, v[52:53], off offset:256
	global_load_dword v99, v[52:53], off offset:512
	global_load_dword v108, v[52:53], off offset:768
	s_waitcnt vmcnt(16)
	v_lshlrev_b32_e32 v54, 16, v50
	v_and_b32_e32 v55, 0xffff0000, v50
	v_lshlrev_b32_e32 v50, 16, v51
	v_and_b32_e32 v51, 0xffff0000, v51
	v_lshlrev_b32_e32 v22, 16, v44
	v_and_b32_e32 v26, 0xffff0000, v45
	v_lshlrev_b32_e32 v56, 16, v47
	v_lshlrev_b32_e32 v42, 16, v46
	v_and_b32_e32 v44, 0xffff0000, v44
	v_lshlrev_b32_e32 v45, 16, v45
	v_and_b32_e32 v47, 0xffff0000, v47
	v_and_b32_e32 v46, 0xffff0000, v46
	s_waitcnt vmcnt(15)
	v_cvt_f32_fp8_e32 v24, v39
	v_cvt_f32_fp8_sdwa v25, v39 src0_sel:BYTE_1
	v_cvt_f32_fp8_sdwa v40, v39 src0_sel:BYTE_2
	v_cvt_f32_fp8_sdwa v41, v39 src0_sel:BYTE_3
	s_waitcnt vmcnt(14)
	v_cvt_f32_fp8_e32 v48, v58
	v_cvt_f32_fp8_sdwa v52, v58 src0_sel:BYTE_1
	v_cvt_f32_fp8_sdwa v60, v58 src0_sel:BYTE_2
	v_cvt_f32_fp8_sdwa v62, v58 src0_sel:BYTE_3
	s_waitcnt vmcnt(13)
	v_cvt_f32_fp8_e32 v39, v61
	v_cvt_f32_fp8_sdwa v64, v61 src0_sel:BYTE_1
	v_cvt_f32_fp8_sdwa v58, v61 src0_sel:BYTE_2
	v_cvt_f32_fp8_sdwa v66, v61 src0_sel:BYTE_3
	s_waitcnt vmcnt(12)
	v_cvt_f32_fp8_e32 v110, v63
	v_cvt_f32_fp8_sdwa v69, v63 src0_sel:BYTE_1
	v_cvt_f32_fp8_sdwa v71, v63 src0_sel:BYTE_2
	v_cvt_f32_fp8_sdwa v73, v63 src0_sel:BYTE_3
	s_waitcnt vmcnt(10)
	v_cvt_f32_fp8_e32 v49, v67
	v_cvt_f32_fp8_sdwa v53, v67 src0_sel:BYTE_1
	v_cvt_f32_fp8_sdwa v61, v67 src0_sel:BYTE_2
	v_cvt_f32_fp8_sdwa v63, v67 src0_sel:BYTE_3
	v_cvt_f32_fp8_e32 v74, v65
	v_cvt_f32_fp8_sdwa v75, v65 src0_sel:BYTE_1
	v_cvt_f32_fp8_sdwa v76, v65 src0_sel:BYTE_2
	v_cvt_f32_fp8_sdwa v77, v65 src0_sel:BYTE_3
	s_waitcnt vmcnt(9)
	v_cvt_f32_fp8_e32 v70, v68
	v_cvt_f32_fp8_sdwa v65, v68 src0_sel:BYTE_1
	v_cvt_f32_fp8_sdwa v72, v68 src0_sel:BYTE_2
	v_cvt_f32_fp8_sdwa v67, v68 src0_sel:BYTE_3
	s_waitcnt vmcnt(8)
	v_cvt_f32_fp8_e32 v78, v79
	v_cvt_f32_fp8_sdwa v81, v79 src0_sel:BYTE_1
	v_cvt_f32_fp8_sdwa v83, v79 src0_sel:BYTE_2
	v_cvt_f32_fp8_sdwa v85, v79 src0_sel:BYTE_3
	s_waitcnt vmcnt(6)
	v_cvt_f32_fp8_e32 v68, v82
	v_cvt_f32_fp8_sdwa v90, v82 src0_sel:BYTE_1
	v_cvt_f32_fp8_sdwa v92, v82 src0_sel:BYTE_2
	v_cvt_f32_fp8_sdwa v94, v82 src0_sel:BYTE_3
	s_waitcnt vmcnt(5)
	v_cvt_f32_fp8_e32 v82, v91
	v_cvt_f32_fp8_sdwa v96, v91 src0_sel:BYTE_1
	v_cvt_f32_fp8_sdwa v84, v91 src0_sel:BYTE_2
	v_cvt_f32_fp8_sdwa v98, v91 src0_sel:BYTE_3
	s_waitcnt vmcnt(4)
	v_cvt_f32_fp8_e32 v79, v93
	v_cvt_f32_fp8_sdwa v112, v93 src0_sel:BYTE_1
	v_cvt_f32_fp8_sdwa v101, v93 src0_sel:BYTE_2
	v_cvt_f32_fp8_sdwa v103, v93 src0_sel:BYTE_3
	s_waitcnt vmcnt(2)
	v_cvt_f32_fp8_sdwa v91, v97 src0_sel:BYTE_1
	v_cvt_f32_fp8_sdwa v93, v97 src0_sel:BYTE_2
	v_cvt_f32_fp8_e32 v86, v80
	v_cvt_f32_fp8_sdwa v87, v80 src0_sel:BYTE_1
	v_cvt_f32_fp8_sdwa v88, v80 src0_sel:BYTE_2
	v_cvt_f32_fp8_sdwa v89, v80 src0_sel:BYTE_3
	v_cvt_f32_fp8_e32 v104, v95
	v_cvt_f32_fp8_sdwa v105, v95 src0_sel:BYTE_1
	v_cvt_f32_fp8_sdwa v106, v95 src0_sel:BYTE_2
	v_cvt_f32_fp8_sdwa v107, v95 src0_sel:BYTE_3
	v_cvt_f32_fp8_sdwa v95, v97 src0_sel:BYTE_3
	v_cvt_f32_fp8_e32 v80, v97
	s_waitcnt vmcnt(1)
	v_cvt_f32_fp8_e32 v100, v99
	v_cvt_f32_fp8_sdwa v97, v99 src0_sel:BYTE_1
	v_cvt_f32_fp8_sdwa v102, v99 src0_sel:BYTE_2
	v_cvt_f32_fp8_sdwa v99, v99 src0_sel:BYTE_3
	s_waitcnt vmcnt(0)
	v_cvt_f32_fp8_e32 v109, v108
	v_cvt_f32_fp8_sdwa v111, v108 src0_sel:BYTE_1
	v_cvt_f32_fp8_sdwa v114, v108 src0_sel:BYTE_2
	v_cvt_f32_fp8_sdwa v108, v108 src0_sel:BYTE_3
	v_pk_mul_f32 v[48:49], v[48:49], s[14:15] op_sel_hi:[1,0]
	v_pk_mul_f32 v[52:53], v[52:53], s[14:15] op_sel_hi:[1,0]
	v_pk_mul_f32 v[60:61], v[60:61], s[14:15] op_sel_hi:[1,0]
	v_pk_mul_f32 v[62:63], v[62:63], s[14:15] op_sel_hi:[1,0]
	v_pk_fma_f32 v[24:25], v[24:25], s[14:15], v[54:55] op_sel_hi:[1,0,1]
	v_pk_fma_f32 v[40:41], v[40:41], s[14:15], v[50:51] op_sel_hi:[1,0,1]
	v_fmac_f32_e32 v56, 0x3d800000, v58
	v_pk_mul_f32 v[64:65], v[64:65], s[14:15] op_sel_hi:[1,0]
	v_pk_mul_f32 v[66:67], v[66:67], s[14:15] op_sel_hi:[1,0]
	v_pk_mul_f32 v[50:51], v[90:91], s[14:15] op_sel_hi:[1,0]
	v_pk_mul_f32 v[54:55], v[92:93], s[14:15] op_sel_hi:[1,0]
	v_add_f32_e32 v22, v48, v22
	v_add_f32_e32 v26, v62, v26
	v_pk_fma_f32 v[24:25], v[74:75], s[14:15], v[24:25] op_sel_hi:[1,0,1]
	v_pk_fma_f32 v[40:41], v[76:77], s[14:15], v[40:41] op_sel_hi:[1,0,1]
	v_mov_b32_e32 v74, v52
	v_mov_b32_e32 v75, v60
	v_fmac_f32_e32 v42, 0x3d800000, v39
	v_fmac_f32_e32 v28, 0x3d800000, v110
	v_pk_mul_f32 v[78:79], v[78:79], s[14:15] op_sel_hi:[1,0]
	v_pk_mul_f32 v[90:91], v[94:95], s[14:15] op_sel_hi:[1,0]
	v_mov_b32_e32 v60, v53
	v_mov_b32_e32 v52, v50
	v_mov_b32_e32 v53, v54
	v_mov_b32_e32 v54, v51
	v_mov_b32_e32 v50, v64
	v_mov_b32_e32 v51, v66
	v_pk_fma_f32 v[56:57], v[72:73], s[14:15], v[56:57] op_sel_hi:[1,0,1]
	v_add_f32_e32 v58, v22, v49
	v_add_f32_e32 v22, v26, v63
	v_pk_fma_f32 v[24:25], v[86:87], s[14:15], v[24:25] op_sel_hi:[1,0,1]
	v_pk_fma_f32 v[40:41], v[88:89], s[14:15], v[40:41] op_sel_hi:[1,0,1]
	v_pk_add_f32 v[44:45], v[74:75], v[44:45]
	v_pk_mul_f32 v[92:93], v[96:97], s[14:15] op_sel_hi:[1,0]
	v_pk_mul_f32 v[94:95], v[98:99], s[14:15] op_sel_hi:[1,0]
	v_add_f32_e32 v28, v28, v78
	v_mov_b32_e32 v66, v65
	v_pk_fma_f32 v[42:43], v[70:71], s[14:15], v[42:43] op_sel_hi:[1,0,1]
	v_pk_add_f32 v[46:47], v[50:51], v[46:47]
	v_pk_fma_f32 v[50:51], v[84:85], s[14:15], v[56:57] op_sel_hi:[1,0,1]
	v_pk_fma_f32 v[24:25], v[104:105], s[14:15], v[24:25] op_sel_hi:[1,0,1]
	v_pk_fma_f32 v[40:41], v[106:107], s[14:15], v[40:41] op_sel_hi:[1,0,1]
	v_pk_add_f32 v[44:45], v[44:45], v[60:61]
	v_add_f32_e32 v22, v22, v90
	v_pk_fma_f32 v[56:57], v[68:69], s[14:15], v[58:59] op_sel_hi:[1,0,1]
	v_mul_f32_e32 v99, 0x3d800000, v108
	v_mov_b32_e32 v64, v92
	v_mov_b32_e32 v65, v94
	v_add_f32_e32 v49, v28, v79
	v_pk_fma_f32 v[42:43], v[82:83], s[14:15], v[42:43] op_sel_hi:[1,0,1]
	v_pk_add_f32 v[46:47], v[46:47], v[66:67]
	v_pk_add_f32 v[44:45], v[44:45], v[52:53]
	v_add_f32_e32 v116, v22, v91
	v_pk_mul_f32 v[52:53], v[40:41], v[40:41]
	v_pk_fma_f32 v[56:57], v[80:81], s[14:15], v[56:57] op_sel_hi:[1,0,1]
	v_mov_b32_e32 v108, v24
	v_mov_b32_e32 v22, v24
	v_mul_f32_e32 v48, v25, v25
	v_mul_f32_e32 v113, 0x3d800000, v112
	v_mul_f32_e32 v97, 0x3d800000, v114
	v_mov_b32_e32 v115, v109
	v_mov_b32_e32 v94, v93
	v_pk_fma_f32 v[42:43], v[100:101], s[14:15], v[42:43] op_sel_hi:[1,0,1]
	v_pk_fma_f32 v[50:51], v[102:103], s[14:15], v[50:51] op_sel_hi:[1,0,1]
	v_pk_add_f32 v[46:47], v[46:47], v[64:65]
	v_mov_b32_e32 v114, v40
	v_mov_b32_e32 v26, v40
	v_pk_add_f32 v[44:45], v[44:45], v[54:55]
	v_pk_fma_f32 v[54:55], v[108:109], v[22:23], v[48:49]
	v_mov_b32_e32 v48, v53
	v_mov_b32_e32 v112, v56
	v_mov_b32_e32 v96, v42
	v_mov_b32_e32 v98, v50
	v_pk_add_f32 v[46:47], v[46:47], v[94:95]
	v_pk_mul_f32 v[52:53], v[56:57], v[56:57]
	v_pk_mul_f32 v[64:65], v[44:45], v[44:45]
	v_pk_fma_f32 v[26:27], v[114:115], v[26:27], v[48:49]
	v_pk_add_f32 v[48:49], v[56:57], v[112:113]
	v_mov_b32_e32 v117, v111
	v_mov_b32_e32 v28, v116
	v_pk_add_f32 v[58:59], v[42:43], v[96:97]
	v_pk_add_f32 v[60:61], v[50:51], v[98:99]
	v_pk_mul_f32 v[66:67], v[46:47], v[46:47]
	v_mov_b32_e32 v110, v44
	v_mov_b32_e32 v22, v44
	v_mov_b32_e32 v53, v49
	v_mov_b32_e32 v48, v65
	v_pk_mul_f32 v[68:69], v[58:59], v[58:59]
	v_pk_mul_f32 v[70:71], v[60:61], v[60:61]
	v_mov_b32_e32 v57, v44
	v_mov_b32_e32 v62, v45
	v_mov_b32_e32 v60, v59
	v_pk_add_f32 v[44:45], v[54:55], v[26:27]
	v_pk_mul_f32 v[26:27], v[54:55], v[26:27]
	v_pk_fma_f32 v[58:59], v[42:43], v[42:43], v[66:67]
	v_pk_fma_f32 v[64:65], v[50:51], v[50:51], v[66:67] op_sel:[0,0,1] op_sel_hi:[1,1,0]
	v_mov_b32_e32 v43, v46
	v_mov_b32_e32 v51, v47
	v_pk_fma_f32 v[46:47], v[110:111], v[22:23], v[52:53]
	v_pk_fma_f32 v[28:29], v[116:117], v[28:29], v[48:49]
	v_mov_b32_e32 v45, v27
	v_pk_add_f32 v[26:27], v[46:47], v[28:29]
	v_pk_mul_f32 v[28:29], v[46:47], v[28:29]
	v_mov_b32_e32 v59, v69
	v_mov_b32_e32 v65, v71
	v_mov_b32_e32 v27, v29
	v_pk_add_f32 v[48:49], v[58:59], v[64:65]
	v_pk_add_f32 v[26:27], v[44:45], v[26:27]
	v_mov_b32_e32 v63, v116
	v_pk_add_f32 v[26:27], v[26:27], v[48:49]
	v_mov_b32_e32 v46, v55
	v_add_f32_e32 v22, v26, v27
	ds_bpermute_b32 v26, v30, v22
	s_waitcnt lgkmcnt(0)
	v_add_f32_e32 v22, v22, v26
	ds_bpermute_b32 v26, v31, v22
	s_waitcnt lgkmcnt(0)
	v_add_f32_e32 v22, v22, v26
	ds_bpermute_b32 v26, v32, v22
	s_waitcnt lgkmcnt(0)
	v_add_f32_e32 v22, v22, v26
	ds_bpermute_b32 v26, v33, v22
	s_waitcnt lgkmcnt(0)
	v_add_f32_e32 v22, v22, v26
	ds_bpermute_b32 v26, v34, v22
	s_waitcnt lgkmcnt(0)
	v_add_f32_e32 v22, v22, v26
	ds_bpermute_b32 v26, v35, v22
	s_waitcnt lgkmcnt(0)
	v_add_f32_e32 v22, v22, v26
	v_fmamk_f32 v22, v22, 0x3a800000, v37
	v_mul_f32_e32 v26, 0x4f800000, v22
	v_cmp_gt_f32_e32 vcc, s3, v22
	s_nop 1
	v_cndmask_b32_e32 v22, v22, v26, vcc
	v_sqrt_f32_e32 v26, v22
	s_nop 0
	v_add_u32_e32 v27, -1, v26
	v_add_u32_e32 v28, 1, v26
	v_fma_f32 v29, -v27, v26, v22
	v_fma_f32 v39, -v28, v26, v22
	v_cmp_ge_f32_e64 s[0:1], 0, v29
	s_nop 1
	v_cndmask_b32_e64 v26, v26, v27, s[0:1]
	v_cmp_lt_f32_e64 s[0:1], 0, v39
	s_nop 1
	v_cndmask_b32_e64 v26, v26, v28, s[0:1]
	v_mul_f32_e32 v27, 0x37800000, v26
	v_cndmask_b32_e32 v26, v26, v27, vcc
	v_cmp_class_f32_e32 vcc, v22, v38
	s_nop 1
	v_cndmask_b32_e32 v22, v26, v22, vcc
	v_div_scale_f32 v26, s[0:1], v22, v22, 1.0
	v_rcp_f32_e32 v28, v26
	v_div_scale_f32 v27, vcc, 1.0, v22, 1.0
	v_fma_f32 v29, -v26, v28, 1.0
	v_fmac_f32_e32 v28, v29, v28
	v_mul_f32_e32 v29, v27, v28
	v_fma_f32 v39, -v26, v29, v27
	v_fmac_f32_e32 v29, v39, v28
	v_fma_f32 v26, -v26, v29, v27
	v_div_fmas_f32 v26, v26, v28, v29
	v_div_fixup_f32 v22, v26, v22, 1.0
	v_pk_mul_f32 v[24:25], v[24:25], v[22:23] op_sel_hi:[1,0]
	v_pk_mul_f32 v[26:27], v[40:41], v[22:23] op_sel_hi:[1,0]
	v_pk_mul_f32 v[28:29], v[56:57], v[22:23] op_sel_hi:[1,0]
	v_pk_mul_f32 v[40:41], v[62:63], v[22:23] op_sel_hi:[1,0]
	v_pk_mul_f32 v[44:45], v[42:43], v[22:23] op_sel_hi:[1,0]
	v_pk_mul_f32 v[48:49], v[50:51], v[22:23] op_sel_hi:[1,0]
	v_pk_mul_f32 v[52:53], v[46:47], v[22:23] op_sel_hi:[1,0]
	v_pk_mul_f32 v[50:51], v[60:61], v[22:23] op_sel_hi:[1,0]
	v_pk_mul_f32 v[26:27], v[2:3], v[26:27]
	v_pk_mul_f32 v[24:25], v[0:1], v[24:25]
	v_pk_mul_f32 v[42:43], v[6:7], v[40:41]
	v_pk_mul_f32 v[40:41], v[4:5], v[28:29]
	v_pk_mul_f32 v[46:47], v[10:11], v[48:49]
	v_pk_mul_f32 v[44:45], v[8:9], v[44:45]
	v_pk_mul_f32 v[50:51], v[14:15], v[50:51]
	v_pk_mul_f32 v[48:49], v[12:13], v[52:53]
	global_store_dwordx4 v[20:21], v[24:27], off offset:-3072 nt
	global_store_dwordx4 v[20:21], v[40:43], off offset:-2048 nt
	global_store_dwordx4 v[20:21], v[44:47], off offset:-1024 nt
	global_store_dwordx4 v[20:21], v[48:51], off nt
	v_lshl_add_u64 v[20:21], v[20:21], 0, s[12:13]
	s_cbranch_scc1 .LBB0_1286
